# baseline (speedup 1.0000x reference)
.Lret2:
	s_getpc_b64 s[40:41]
.Lwpc:
	v_mbcnt_lo_u32_b32 v243, -1, 0
	s_mov_b32 s38, .Lfunc_end0-.Lwpc
	v_mbcnt_hi_u32_b32 v243, -1, v243
	v_lshlrev_b32_e32 v243, 7, v243
	v_cmp_gt_u32_e64 s[38:39], s38, v243
	s_and_saveexec_b64 s[42:43], s[38:39]
	global_load_dword v242, v243, s[40:41]
	s_mov_b64 exec, s[42:43]
	v_lshrrev_b32_e32 v151, 4, v120
	v_lshl_add_u32 v152, v123, 4, v131
	v_lshlrev_b32_e32 v153, 4, v123
	v_lshlrev_b32_e32 v154, 1, v121
	v_lshrrev_b32_e32 v155, 4, v122
	v_lshl_add_u32 v152, v151, 2, v152
	v_or_b32_e32 v155, v154, v155
	v_sub_u32_e32 v174, 11, v154
	v_lshl_or_b32 v156, v155, 8, v153
	v_cvt_f32_i32_e32 v174, v174
	v_cmp_lt_u32_e32 vcc, 31, v0
	v_add_u32_e32 v157, 0x4c00, v156
	v_mul_f32_e32 v175, 0xbf38aa3b, v174
	v_add_u32_e32 v158, 0xe400, v156
	v_mul_f32_e32 v175, v175, v174
	v_exp_f32_e32 v175, v175
	s_nop 0
	v_cndmask_b32_e32 v174, 1.0, v175, vcc
	s_waitcnt vmcnt(10)
	v_cvt_pk_f16_f32 v79, v8, v9
	v_cvt_pk_f16_f32 v78, v6, v7
	ds_write_b64 v141, v[78:79] offset:19456
	s_waitcnt vmcnt(9)
	v_cvt_pk_f16_f32 v79, v12, v13
	v_cvt_pk_f16_f32 v78, v10, v11
	ds_write_b64 v143, v[78:79] offset:19456
	s_waitcnt vmcnt(8)
	v_cvt_pk_f16_f32 v79, v20, v21
	v_cvt_pk_f16_f32 v78, v18, v19
	ds_write_b64 v144, v[78:79] offset:19456
	s_waitcnt vmcnt(7)
	v_cvt_pk_f16_f32 v79, v24, v25
	v_cvt_pk_f16_f32 v78, v22, v23
	ds_write_b64 v145, v[78:79] offset:19456
	s_waitcnt vmcnt(6)
	v_cvt_pk_f16_f32 v79, v28, v29
	v_cvt_pk_f16_f32 v78, v26, v27
	ds_write_b64 v146, v[78:79] offset:19456
	s_waitcnt vmcnt(5)
	v_cvt_pk_f16_f32 v79, v32, v33
	v_cvt_pk_f16_f32 v78, v30, v31
	ds_write_b64 v147, v[78:79] offset:19456
	s_waitcnt vmcnt(4)
	v_cvt_pk_f16_f32 v79, v40, v41
	v_cvt_pk_f16_f32 v78, v38, v39
	ds_write_b64 v141, v[78:79] offset:22568
	s_waitcnt vmcnt(3)
	v_cvt_pk_f16_f32 v79, v44, v45
	v_cvt_pk_f16_f32 v78, v42, v43
	ds_write_b64 v148, v[78:79] offset:19456
	s_waitcnt vmcnt(2)
	v_cvt_pk_f16_f32 v79, v52, v53
	v_cvt_pk_f16_f32 v78, v50, v51
	ds_write_b64 v149, v[78:79] offset:19456
	s_mov_b32 s3, 3
	v_mov_b32_e32 v86, 0
	v_mov_b32_e32 v78, 0
	v_mov_b32_e32 v79, 0
	v_mov_b32_e32 v80, 0
	v_mov_b32_e32 v81, 0
	v_mov_b32_e32 v82, 0
	v_mov_b32_e32 v83, 0
	v_mov_b32_e32 v84, 0
	v_mov_b32_e32 v85, 0
	ds_read_b128 v[194:197], v142
	ds_read_b128 v[198:201], v136
	ds_read_b128 v[202:205], v136 offset:9728
	ds_read_b128 v[206:209], v142 offset:64
	ds_read_b128 v[210:213], v136 offset:64
	ds_read_b128 v[214:217], v136 offset:9792
	ds_read_b128 v[218:221], v142 offset:128
	ds_read_b128 v[222:225], v136 offset:128
	ds_read_b128 v[226:229], v136 offset:9856
	ds_read_b128 v[230:233], v142 offset:192
	ds_read_b128 v[234:237], v136 offset:192
	ds_read_b128 v[238:241], v136 offset:9920
	s_waitcnt lgkmcnt(9)
	v_mfma_f32_16x16x32_f16 v[78:81], v[194:197], v[198:201], v[78:81]
	v_dot2c_f32_f16_e32 v86, v194, v194
	v_dot2c_f32_f16_e32 v86, v195, v195
	v_mfma_f32_16x16x32_f16 v[82:85], v[194:197], v[202:205], v[82:85]
	v_dot2c_f32_f16_e32 v86, v196, v196
	v_dot2c_f32_f16_e32 v86, v197, v197
	ds_read_b128 v[194:197], v142 offset:256
	ds_read_b128 v[198:201], v136 offset:256
	ds_read_b128 v[202:205], v136 offset:9984
	s_waitcnt lgkmcnt(9)
	v_mfma_f32_16x16x32_f16 v[78:81], v[206:209], v[210:213], v[78:81]
	v_dot2c_f32_f16_e32 v86, v206, v206
	v_dot2c_f32_f16_e32 v86, v207, v207
	v_mfma_f32_16x16x32_f16 v[82:85], v[206:209], v[214:217], v[82:85]
	v_dot2c_f32_f16_e32 v86, v208, v208
	v_dot2c_f32_f16_e32 v86, v209, v209
	ds_read_b128 v[206:209], v142 offset:320
	ds_read_b128 v[210:213], v136 offset:320
	ds_read_b128 v[214:217], v136 offset:10048
	s_waitcnt lgkmcnt(9)
	v_mfma_f32_16x16x32_f16 v[78:81], v[218:221], v[222:225], v[78:81]
	v_dot2c_f32_f16_e32 v86, v218, v218
	v_dot2c_f32_f16_e32 v86, v219, v219
	v_mfma_f32_16x16x32_f16 v[82:85], v[218:221], v[226:229], v[82:85]
	v_dot2c_f32_f16_e32 v86, v220, v220
	v_dot2c_f32_f16_e32 v86, v221, v221
	s_waitcnt lgkmcnt(6)
	v_mfma_f32_16x16x32_f16 v[78:81], v[230:233], v[234:237], v[78:81]
	v_dot2c_f32_f16_e32 v86, v230, v230
	v_dot2c_f32_f16_e32 v86, v231, v231
	v_mfma_f32_16x16x32_f16 v[82:85], v[230:233], v[238:241], v[82:85]
	v_dot2c_f32_f16_e32 v86, v232, v232
	v_dot2c_f32_f16_e32 v86, v233, v233
	s_waitcnt lgkmcnt(3)
	v_mfma_f32_16x16x32_f16 v[78:81], v[194:197], v[198:201], v[78:81]
	v_dot2c_f32_f16_e32 v86, v194, v194
	v_dot2c_f32_f16_e32 v86, v195, v195
	v_mfma_f32_16x16x32_f16 v[82:85], v[194:197], v[202:205], v[82:85]
	v_dot2c_f32_f16_e32 v86, v196, v196
	v_dot2c_f32_f16_e32 v86, v197, v197
	s_waitcnt lgkmcnt(0)
	v_mfma_f32_16x16x32_f16 v[78:81], v[206:209], v[210:213], v[78:81]
	v_dot2c_f32_f16_e32 v86, v206, v206
	v_dot2c_f32_f16_e32 v86, v207, v207
	v_mfma_f32_16x16x32_f16 v[82:85], v[206:209], v[214:217], v[82:85]
	v_dot2c_f32_f16_e32 v86, v208, v208
	v_dot2c_f32_f16_e32 v86, v209, v209
	ds_read_b128 v[222:225], v136 offset:384
	ds_read_b128 v[226:229], v136 offset:10112
	ds_read_b128 v[234:237], v136 offset:448
	ds_read_b128 v[238:241], v136 offset:10176
	ds_read_b128 v[198:201], v136 offset:512
	ds_read_b128 v[202:205], v136 offset:10240
	ds_read2st64_b64 v[88:91], v160 offset0:1 offset1:20
	s_waitcnt vmcnt(1)
	v_cvt_pk_f16_f32 v163, v188, v189
	v_cvt_pk_f16_f32 v162, v186, v187
	s_and_saveexec_b64 s[12:13], s[8:9]
	ds_write_b64 v150, v[162:163] offset:19456
	s_or_b64 exec, exec, s[12:13]
	ds_read_b128 v[218:221], v142 offset:384
	ds_read_b128 v[230:233], v142 offset:448
	ds_read_b128 v[194:197], v142 offset:512
	ds_read_b64 v[92:93], v159 offset:20032
	s_waitcnt lgkmcnt(3)
	v_mfma_f32_16x16x32_f16 v[78:81], v[218:221], v[222:225], v[78:81]
	v_dot2c_f32_f16_e32 v86, v218, v218
	v_dot2c_f32_f16_e32 v86, v219, v219
	v_mfma_f32_16x16x32_f16 v[82:85], v[218:221], v[226:229], v[82:85]
	v_dot2c_f32_f16_e32 v86, v220, v220
	v_dot2c_f32_f16_e32 v86, v221, v221
	s_waitcnt lgkmcnt(2)
	v_mfma_f32_16x16x32_f16 v[78:81], v[230:233], v[234:237], v[78:81]
	v_dot2c_f32_f16_e32 v86, v230, v230
	v_dot2c_f32_f16_e32 v86, v231, v231
	v_mfma_f32_16x16x32_f16 v[82:85], v[230:233], v[238:241], v[82:85]
	v_dot2c_f32_f16_e32 v86, v232, v232
	v_dot2c_f32_f16_e32 v86, v233, v233
	s_waitcnt lgkmcnt(1)
	v_mfma_f32_16x16x32_f16 v[78:81], v[194:197], v[198:201], v[78:81]
	v_dot2c_f32_f16_e32 v86, v194, v194
	v_dot2c_f32_f16_e32 v86, v195, v195
	v_mfma_f32_16x16x32_f16 v[82:85], v[194:197], v[202:205], v[82:85]
	v_dot2c_f32_f16_e32 v86, v196, v196
	v_dot2c_f32_f16_e32 v86, v197, v197
	s_waitcnt lgkmcnt(0)
	v_mfma_f32_16x16x16_f16 v[78:81], v[92:93], v[88:89], v[78:81]
	v_dot2c_f32_f16_e32 v86, v92, v92
	v_dot2c_f32_f16_e32 v86, v93, v93
	v_mfma_f32_16x16x16_f16 v[82:85], v[92:93], v[90:91], v[82:85]
	s_branch .Lnorm

.LBB0_24:
	s_waitcnt vmcnt(0)
	s_or_b64 exec, exec, s[0:1]
	v_cmp_eq_u32_e32 vcc, 0, v0
	s_waitcnt lgkmcnt(0)
	s_barrier
	s_and_saveexec_b64 s[0:1], vcc
	s_cbranch_execz .LBB0_26
	v_mov_b32_e32 v0, 0x18000
	ds_read_b128 v[0:3], v0
	v_mov_b32_e32 v4, 0x18010
	ds_read_b128 v[4:7], v4
	s_ashr_i32 s3, s2, 31
	s_lshl_b64 s[0:1], s[2:3], 2
	s_waitcnt lgkmcnt(0)
	v_add_f32_e32 v0, v0, v1
	v_add_f32_e32 v2, v2, v3
	v_add_f32_e32 v4, v4, v5
	v_add_f32_e32 v6, v6, v7
	v_add_f32_e32 v0, v0, v2
	v_add_f32_e32 v4, v4, v6
	v_add_f32_e32 v0, v0, v4
	s_add_u32 s0, s14, s0
	v_mul_f32_e32 v0, 0x3be32166, v0
	s_addc_u32 s1, s15, s1
	v_mov_b32_e32 v1, 0
	global_store_dword v1, v0, s[0:1]

	.amdhsa_kernel _Z11knrm_kernelPKfS0_PKiS2_S0_Pf
		.amdhsa_group_segment_fixed_size 99712
		.amdhsa_private_segment_fixed_size 0
		.amdhsa_kernarg_size 48
		.amdhsa_user_sgpr_count 2
		.amdhsa_user_sgpr_dispatch_ptr 0
		.amdhsa_user_sgpr_queue_ptr 0
		.amdhsa_user_sgpr_kernarg_segment_ptr 1
		.amdhsa_user_sgpr_dispatch_id 0
		.amdhsa_user_sgpr_kernarg_preload_length 0
		.amdhsa_user_sgpr_kernarg_preload_offset 0
		.amdhsa_user_sgpr_private_segment_size 0
		.amdhsa_uses_dynamic_stack 0
		.amdhsa_enable_private_segment 0
		.amdhsa_system_sgpr_workgroup_id_x 1
		.amdhsa_system_sgpr_workgroup_id_y 0
		.amdhsa_system_sgpr_workgroup_id_z 0
		.amdhsa_system_sgpr_workgroup_info 0
		.amdhsa_system_vgpr_workitem_id 0
		.amdhsa_next_free_vgpr 244
		.amdhsa_next_free_sgpr 96
		.amdhsa_accum_offset 244
		.amdhsa_reserve_vcc 1
		.amdhsa_float_round_mode_32 0
		.amdhsa_float_round_mode_16_64 0
		.amdhsa_float_denorm_mode_32 3
		.amdhsa_float_denorm_mode_16_64 3
		.amdhsa_dx10_clamp 1
		.amdhsa_ieee_mode 1
		.amdhsa_fp16_overflow 0
		.amdhsa_tg_split 0
		.amdhsa_exception_fp_ieee_invalid_op 0
		.amdhsa_exception_fp_denorm_src 0
		.amdhsa_exception_fp_ieee_div_zero 0
		.amdhsa_exception_fp_ieee_overflow 0
		.amdhsa_exception_fp_ieee_underflow 0
		.amdhsa_exception_fp_ieee_inexact 0
		.amdhsa_exception_int_div_zero 0
	.end_amdhsa_kernel

amdhsa.kernels:
  - .agpr_count:     0
    .args:
      - .actual_access:  read_only
        .address_space:  global
        .offset:         0
        .size:           8
        .value_kind:     global_buffer
      - .actual_access:  read_only
        .address_space:  global
        .offset:         8
        .size:           8
        .value_kind:     global_buffer
      - .actual_access:  read_only
        .address_space:  global
        .offset:         16
        .size:           8
        .value_kind:     global_buffer
      - .actual_access:  read_only
        .address_space:  global
        .offset:         24
        .size:           8
        .value_kind:     global_buffer
      - .actual_access:  read_only
        .address_space:  global
        .offset:         32
        .size:           8
        .value_kind:     global_buffer
      - .actual_access:  write_only
        .address_space:  global
        .offset:         40
        .size:           8
        .value_kind:     global_buffer
    .group_segment_fixed_size: 99712
    .kernarg_segment_align: 8
    .kernarg_segment_size: 48
    .language:       OpenCL C
    .language_version:
      - 2
      - 0
    .max_flat_workgroup_size: 512
    .name:           _Z11knrm_kernelPKfS0_PKiS2_S0_Pf
    .private_segment_fixed_size: 0
    .sgpr_count:     32
    .sgpr_spill_count: 0
    .symbol:         _Z11knrm_kernelPKfS0_PKiS2_S0_Pf.kd
    .uniform_work_group_size: 1
    .uses_dynamic_stack: false
    .vgpr_count:     244
    .vgpr_spill_count: 0
    .wavefront_size: 64
